# layer-0 gate weights staged into LDS with 16 wide loads in flight per thread (was 16 serialized load->wait->store trips); plus no-setprio, phase-11 reorder, attention prefetch fix
# speedup vs baseline: 1.0096x; 1.0048x over previous
.Lstage_gates:
	v_and_b32_e32 v10, 3, v0
	v_lshrrev_b32_e32 v11, 2, v0
	v_mad_u64_u32 v[12:13], s[6:7], v11, s2, v[6:7]
	v_lshlrev_b32_e32 v14, 4, v10
	v_add_u32_e32 v14, 0x6000, v14
	v_mov_b32_e32 v15, 0
	v_lshl_add_u64 v[12:13], v[12:13], 0, v[14:15]
	s_mov_b32 s6, 0x302000
	s_mov_b32 s7, 0
	v_lshlrev_b32_e32 v16, 15, v10
	v_lshl_add_u32 v16, v11, 2, v16
	global_load_dwordx4 v[20:23], v[12:13], off
	v_lshl_add_u64 v[12:13], v[12:13], 0, s[6:7]
	global_load_dwordx4 v[24:27], v[12:13], off
	v_lshl_add_u64 v[12:13], v[12:13], 0, s[6:7]
	global_load_dwordx4 v[28:31], v[12:13], off
	v_lshl_add_u64 v[12:13], v[12:13], 0, s[6:7]
	global_load_dwordx4 v[32:35], v[12:13], off
	v_lshl_add_u64 v[12:13], v[12:13], 0, s[6:7]
	global_load_dwordx4 v[36:39], v[12:13], off
	v_lshl_add_u64 v[12:13], v[12:13], 0, s[6:7]
	global_load_dwordx4 v[40:43], v[12:13], off
	v_lshl_add_u64 v[12:13], v[12:13], 0, s[6:7]
	global_load_dwordx4 v[44:47], v[12:13], off
	v_lshl_add_u64 v[12:13], v[12:13], 0, s[6:7]
	global_load_dwordx4 v[48:51], v[12:13], off
	v_lshl_add_u64 v[12:13], v[12:13], 0, s[6:7]
	global_load_dwordx4 v[52:55], v[12:13], off
	v_lshl_add_u64 v[12:13], v[12:13], 0, s[6:7]
	global_load_dwordx4 v[56:59], v[12:13], off
	v_lshl_add_u64 v[12:13], v[12:13], 0, s[6:7]
	global_load_dwordx4 v[60:63], v[12:13], off
	v_lshl_add_u64 v[12:13], v[12:13], 0, s[6:7]
	global_load_dwordx4 v[64:67], v[12:13], off
	v_lshl_add_u64 v[12:13], v[12:13], 0, s[6:7]
	global_load_dwordx4 v[68:71], v[12:13], off
	v_lshl_add_u64 v[12:13], v[12:13], 0, s[6:7]
	global_load_dwordx4 v[72:75], v[12:13], off
	v_lshl_add_u64 v[12:13], v[12:13], 0, s[6:7]
	global_load_dwordx4 v[76:79], v[12:13], off
	v_lshl_add_u64 v[12:13], v[12:13], 0, s[6:7]
	global_load_dwordx4 v[80:83], v[12:13], off
	s_waitcnt vmcnt(15)
	ds_write_b32 v16, v20 offset:0
	ds_write_b32 v16, v21 offset:8192
	ds_write_b32 v16, v22 offset:16384
	ds_write_b32 v16, v23 offset:24576
	s_waitcnt vmcnt(14)
	ds_write_b32 v16, v24 offset:512
	ds_write_b32 v16, v25 offset:8704
	ds_write_b32 v16, v26 offset:16896
	ds_write_b32 v16, v27 offset:25088
	s_waitcnt vmcnt(13)
	ds_write_b32 v16, v28 offset:1024
	ds_write_b32 v16, v29 offset:9216
	ds_write_b32 v16, v30 offset:17408
	ds_write_b32 v16, v31 offset:25600
	s_waitcnt vmcnt(12)
	ds_write_b32 v16, v32 offset:1536
	ds_write_b32 v16, v33 offset:9728
	ds_write_b32 v16, v34 offset:17920
	ds_write_b32 v16, v35 offset:26112
	s_waitcnt vmcnt(11)
	ds_write_b32 v16, v36 offset:2048
	ds_write_b32 v16, v37 offset:10240
	ds_write_b32 v16, v38 offset:18432
	ds_write_b32 v16, v39 offset:26624
	s_waitcnt vmcnt(10)
	ds_write_b32 v16, v40 offset:2560
	ds_write_b32 v16, v41 offset:10752
	ds_write_b32 v16, v42 offset:18944
	ds_write_b32 v16, v43 offset:27136
	s_waitcnt vmcnt(9)
	ds_write_b32 v16, v44 offset:3072
	ds_write_b32 v16, v45 offset:11264
	ds_write_b32 v16, v46 offset:19456
	ds_write_b32 v16, v47 offset:27648
	s_waitcnt vmcnt(8)
	ds_write_b32 v16, v48 offset:3584
	ds_write_b32 v16, v49 offset:11776
	ds_write_b32 v16, v50 offset:19968
	ds_write_b32 v16, v51 offset:28160
	s_waitcnt vmcnt(7)
	ds_write_b32 v16, v52 offset:4096
	ds_write_b32 v16, v53 offset:12288
	ds_write_b32 v16, v54 offset:20480
	ds_write_b32 v16, v55 offset:28672
	s_waitcnt vmcnt(6)
	ds_write_b32 v16, v56 offset:4608
	ds_write_b32 v16, v57 offset:12800
	ds_write_b32 v16, v58 offset:20992
	ds_write_b32 v16, v59 offset:29184
	s_waitcnt vmcnt(5)
	ds_write_b32 v16, v60 offset:5120
	ds_write_b32 v16, v61 offset:13312
	ds_write_b32 v16, v62 offset:21504
	ds_write_b32 v16, v63 offset:29696
	s_waitcnt vmcnt(4)
	ds_write_b32 v16, v64 offset:5632
	ds_write_b32 v16, v65 offset:13824
	ds_write_b32 v16, v66 offset:22016
	ds_write_b32 v16, v67 offset:30208
	s_waitcnt vmcnt(3)
	ds_write_b32 v16, v68 offset:6144
	ds_write_b32 v16, v69 offset:14336
	ds_write_b32 v16, v70 offset:22528
	ds_write_b32 v16, v71 offset:30720
	s_waitcnt vmcnt(2)
	ds_write_b32 v16, v72 offset:6656
	ds_write_b32 v16, v73 offset:14848
	ds_write_b32 v16, v74 offset:23040
	ds_write_b32 v16, v75 offset:31232
	s_waitcnt vmcnt(1)
	ds_write_b32 v16, v76 offset:7168
	ds_write_b32 v16, v77 offset:15360
	ds_write_b32 v16, v78 offset:23552
	ds_write_b32 v16, v79 offset:31744
	s_waitcnt vmcnt(0)
	ds_write_b32 v16, v80 offset:7680
	ds_write_b32 v16, v81 offset:15872
	ds_write_b32 v16, v82 offset:24064
	ds_write_b32 v16, v83 offset:32256
	s_or_b64 exec, exec, s[0:1]
	v_cmp_eq_u32_e64 s[4:5], 2, 0
	s_and_saveexec_b64 s[0:1], s[4:5]
	v_readlane_b32 s96, v254, 60
	v_readlane_b32 s97, v254, 61
	s_cbranch_execz .LBB0_185
	v_readlane_b32 s52, v254, 7
	v_readlane_b32 s56, v254, 11
	v_readlane_b32 s57, v254, 12
	v_lshrrev_b32_e32 v1, 4, v5
	v_lshrrev_b32_e32 v9, 4, v4
	s_movk_i32 s2, 0x6040
	v_mov_b64_e32 v[4:5], s[56:57]
	v_mad_u64_u32 v[6:7], s[4:5], v9, s2, v[4:5]
	v_mov_b32_e32 v135, 0
	v_lshl_add_u64 v[6:7], v[6:7], 0, v[134:135]
	v_mad_u64_u32 v[4:5], s[4:5], v1, s2, v[4:5]
	v_add_co_u32_e32 v6, vcc, 0x6000, v6
	v_lshl_add_u64 v[4:5], v[4:5], 0, v[134:135]
	s_nop 0
	v_addc_co_u32_e32 v7, vcc, 0, v7, vcc
	v_add_co_u32_e32 v4, vcc, 0x6000, v4
	v_readlane_b32 s53, v254, 8
	s_nop 0
	v_addc_co_u32_e32 v5, vcc, 0, v5, vcc
	global_load_dword v6, v[6:7], off
	s_nop 0
	global_load_dword v4, v[4:5], off
	v_lshl_add_u32 v5, v9, 2, v3
	v_readlane_b32 s54, v254, 9
	v_readlane_b32 s55, v254, 10
	v_readlane_b32 s58, v254, 13
	v_readlane_b32 s59, v254, 14
	v_readlane_b32 s60, v254, 15
	v_readlane_b32 s61, v254, 16
	v_readlane_b32 s62, v254, 17
	v_readlane_b32 s63, v254, 18
	v_readlane_b32 s64, v254, 19
	v_readlane_b32 s65, v254, 20
	v_readlane_b32 s66, v254, 21
	v_readlane_b32 s67, v254, 22
	v_lshl_add_u32 v1, v1, 2, v3
	s_waitcnt vmcnt(1)
	ds_write_b32 v5, v6
	s_waitcnt vmcnt(0)
	ds_write_b32 v1, v4
